# J1 + the three loop-counter increments moved from the latch into the s_nop 4 slot at the softmax segment head (3 SALU + s_nop 1 = same 5 wait states)
# speedup vs baseline: 1.0257x; 1.0003x over previous
.LBB0_1613:
	s_add_i32 s14, s13, 1
	s_cmp_lg_u32 s13, 2
	s_cselect_b32 s13, s14, 0
	s_add_i32 s14, s17, 1
	s_cmp_lg_u32 s17, 2
	s_cselect_b32 s17, s14, 0
	s_add_i32 s14, s16, 1
	s_cmp_lg_u32 s16, 2
	s_cselect_b32 s16, s14, 0
	s_cmp_eq_u32 s19, 0x200000
	s_cbranch_scc1 .LBB0_1622

.LBB0_1616:
	s_add_i32 s18, s18, 1
	s_addk_i32 s19, 0x2000
	s_addk_i32 s20, 0x3000
	s_nop 1
	v_exp_f32_e32 v80, v80
	v_exp_f32_e32 v81, v81
	v_exp_f32_e32 v82, v82
	v_exp_f32_e32 v83, v83
	v_add_f32_e32 v144, 0, v80
	v_exp_f32_e32 v84, v84
	v_add_f32_e32 v144, v81, v144
	v_exp_f32_e32 v85, v85
	v_add_f32_e32 v144, v82, v144
	v_exp_f32_e32 v86, v86
	v_add_f32_e32 v144, v83, v144
	v_exp_f32_e32 v87, v87
	v_add_f32_e32 v144, v84, v144
	v_exp_f32_e32 v88, v88
	v_add_f32_e32 v144, v85, v144
	v_exp_f32_e32 v89, v89
	v_add_f32_e32 v144, v86, v144
	v_exp_f32_e32 v90, v90
	v_add_f32_e32 v144, v87, v144
	v_exp_f32_e32 v91, v91
	v_add_f32_e32 v144, v88, v144
	v_exp_f32_e32 v92, v92
	v_add_f32_e32 v144, v89, v144
	v_exp_f32_e32 v93, v93
	v_add_f32_e32 v144, v90, v144
	v_exp_f32_e32 v94, v94
	v_add_f32_e32 v144, v91, v144
	v_exp_f32_e32 v95, v95
	v_add_f32_e32 v144, v92, v144
	v_exp_f32_e32 v96, v96
	v_add_f32_e32 v144, v93, v144
	v_exp_f32_e32 v97, v97
	v_add_f32_e32 v144, v94, v144
	v_exp_f32_e32 v98, v98
	v_add_f32_e32 v144, v95, v144
	v_exp_f32_e32 v99, v99
	v_add_f32_e32 v144, v96, v144
	v_exp_f32_e32 v100, v100
	v_add_f32_e32 v144, v97, v144
	v_exp_f32_e32 v101, v101
	v_add_f32_e32 v144, v98, v144
	v_exp_f32_e32 v102, v102
	v_add_f32_e32 v144, v99, v144
	v_exp_f32_e32 v103, v103
	v_add_f32_e32 v144, v100, v144
	v_exp_f32_e32 v104, v104
	v_add_f32_e32 v144, v101, v144
	v_exp_f32_e32 v105, v105
	v_add_f32_e32 v144, v102, v144
	v_exp_f32_e32 v106, v106
	v_add_f32_e32 v144, v103, v144
	v_exp_f32_e32 v107, v107
	v_add_f32_e32 v144, v104, v144
	v_exp_f32_e32 v108, v108
	v_add_f32_e32 v144, v105, v144
	v_exp_f32_e32 v109, v109
	v_add_f32_e32 v144, v106, v144
	v_exp_f32_e32 v110, v110
	v_add_f32_e32 v144, v107, v144
	v_exp_f32_e32 v111, v111
	v_add_f32_e32 v144, v108, v144
	v_add_f32_e32 v144, v109, v144
	v_add_f32_e32 v144, v110, v144
	v_add_f32_e32 v186, v111, v144
	v_cmp_ge_f32_e32 vcc, s58, v186
	s_cmp_eq_u64 vcc, exec
	s_cbranch_scc0 .LBB0_1619
